# speedup vs baseline: 1.0065x; 1.0065x over previous
.Lh_loop_first:
	ds_read_b32 v24, v26
	s_sub_i32 s49, s44, s43
	s_sub_i32 s50, s45, s43
	s_add_i32 s43, s43, 64
	v_add_u32_e32 v26, 0x100, v26
	s_waitcnt lgkmcnt(0)
	v_fmamk_f32 v27, v24, 0x42000000, v41
	v_rndne_f32_e32 v28, v27
	v_cmp_le_i32_e32 vcc, s49, v1
	v_cmp_le_i32_e64 s[52:53], s50, v1
	v_sub_f32_e32 v29, v27, v28
	v_cvt_i32_f32_e32 v30, v28
	v_cndmask_b32_e32 v36, v38, v39, vcc
	v_mul_f32_e32 v37, 0xbf38aa3b, v29
	v_cndmask_b32_e64 v36, v36, v40, s[52:53]
	v_fmamk_f32 v32, v29, 0x3fb8aa3b, v42
	v_fma_f32 v33, -v29, s51, v42
	v_fmaak_f32 v31, v29, v37, 0x41a00000
	v_lshl_add_u32 v30, v30, 6, v36
	v_exp_f32_e32 v31, v31
	v_exp_f32_e32 v32, v32
	v_exp_f32_e32 v33, v33
.Lh_loop_body:
	ds_read_b32 v24, v26
	s_sub_i32 s59, s42, s43
	s_sub_i32 s49, s44, s43
	s_sub_i32 s50, s45, s43
	s_cmp_ge_i32 s59, 64
	s_cselect_b32 s60, 1, 0
	s_lshl_b32 s61, s60, 6
	s_lshl_b32 s62, s60, 8
	s_add_i32 s43, s43, s61
	v_cvt_rpi_i32_f32_e32 v64, v31
	ds_add_u32 v30, v64 offset:320
	v_mul_f32_e32 v34, v32, v31
	v_mul_f32_e32 v35, v33, v31
	v_cvt_rpi_i32_f32_e32 v64, v34
	v_cvt_rpi_i32_f32_e32 v65, v35
	ds_add_u32 v30, v64 offset:384
	ds_add_u32 v30, v65 offset:256
	v_add_u32_e32 v26, s62, v26
	s_waitcnt lgkmcnt(3)
	v_fmamk_f32 v27, v24, 0x42000000, v41
	v_mul_f32_e32 v32, 0x3ebc5ab2, v32
	v_mul_f32_e32 v33, 0x3ebc5ab2, v33
	v_rndne_f32_e32 v28, v27
	v_mul_f32_e32 v34, v32, v34
	v_mul_f32_e32 v35, v33, v35
	v_cmp_le_i32_e32 vcc, s49, v1
	v_cvt_rpi_i32_f32_e32 v64, v34
	v_cvt_rpi_i32_f32_e32 v65, v35
	v_cmp_le_i32_e64 s[52:53], s50, v1
	ds_add_u32 v30, v64 offset:448
	ds_add_u32 v30, v65 offset:192
	v_sub_f32_e32 v29, v27, v28
	v_mul_f32_e32 v32, 0x3ebc5ab2, v32
	v_mul_f32_e32 v33, 0x3ebc5ab2, v33
	v_cvt_i32_f32_e32 v60, v28
	v_mul_f32_e32 v34, v32, v34
	v_mul_f32_e32 v35, v33, v35
	v_cndmask_b32_e32 v36, v38, v39, vcc
	v_cvt_rpi_i32_f32_e32 v64, v34
	v_cvt_rpi_i32_f32_e32 v65, v35
	v_mul_f32_e32 v37, 0xbf38aa3b, v29
	ds_add_u32 v30, v64 offset:512
	ds_add_u32 v30, v65 offset:128
	v_cndmask_b32_e64 v36, v36, v40, s[52:53]
	v_mul_f32_e32 v32, 0x3ebc5ab2, v32
	v_mul_f32_e32 v33, 0x3ebc5ab2, v33
	v_fmamk_f32 v62, v29, 0x3fb8aa3b, v42
	v_mul_f32_e32 v34, v32, v34
	v_mul_f32_e32 v35, v33, v35
	v_fma_f32 v63, -v29, s51, v42
	v_cvt_rpi_i32_f32_e32 v64, v34
	v_cvt_rpi_i32_f32_e32 v65, v35
	v_fmaak_f32 v61, v29, v37, 0x41a00000
	ds_add_u32 v30, v64 offset:576
	ds_add_u32 v30, v65 offset:64
	v_lshl_add_u32 v60, v60, 6, v36
	v_mul_f32_e32 v32, 0x3ebc5ab2, v32
	v_mul_f32_e32 v33, 0x3ebc5ab2, v33
	v_exp_f32_e32 v61, v61
	v_mul_f32_e32 v34, v32, v34
	v_mul_f32_e32 v35, v33, v35
	v_exp_f32_e32 v62, v62
	v_cvt_rpi_i32_f32_e32 v64, v34
	v_cvt_rpi_i32_f32_e32 v65, v35
	v_exp_f32_e32 v63, v63
	ds_add_u32 v30, v64 offset:640
	ds_add_u32 v30, v65
	v_mov_b32_e32 v30, v60
	v_mov_b32_e32 v31, v61
	v_mov_b32_e32 v32, v62
	v_mov_b32_e32 v33, v63
	s_cmp_lg_u32 s60, 0
	s_cbranch_scc1 .Lh_loop_body

	.amdhsa_kernel _Z6k_histPKfS0_S0_PfPiS1_
		.amdhsa_group_segment_fixed_size 32
		.amdhsa_private_segment_fixed_size 0
		.amdhsa_kernarg_size 48
		.amdhsa_user_sgpr_count 2
		.amdhsa_user_sgpr_dispatch_ptr 0
		.amdhsa_user_sgpr_queue_ptr 0
		.amdhsa_user_sgpr_kernarg_segment_ptr 1
		.amdhsa_user_sgpr_dispatch_id 0
		.amdhsa_user_sgpr_kernarg_preload_length 0
		.amdhsa_user_sgpr_kernarg_preload_offset 0
		.amdhsa_user_sgpr_private_segment_size 0
		.amdhsa_uses_dynamic_stack 0
		.amdhsa_enable_private_segment 0
		.amdhsa_system_sgpr_workgroup_id_x 1
		.amdhsa_system_sgpr_workgroup_id_y 0
		.amdhsa_system_sgpr_workgroup_id_z 0
		.amdhsa_system_sgpr_workgroup_info 0
		.amdhsa_system_vgpr_workitem_id 0
		.amdhsa_next_free_vgpr 66
		.amdhsa_next_free_sgpr 64
		.amdhsa_accum_offset 68
		.amdhsa_reserve_vcc 1
		.amdhsa_float_round_mode_32 0
		.amdhsa_float_round_mode_16_64 0
		.amdhsa_float_denorm_mode_32 3
		.amdhsa_float_denorm_mode_16_64 3
		.amdhsa_dx10_clamp 1
		.amdhsa_ieee_mode 1
		.amdhsa_fp16_overflow 0
		.amdhsa_tg_split 0
		.amdhsa_exception_fp_ieee_invalid_op 0
		.amdhsa_exception_fp_denorm_src 0
		.amdhsa_exception_fp_ieee_div_zero 0
		.amdhsa_exception_fp_ieee_overflow 0
		.amdhsa_exception_fp_ieee_underflow 0
		.amdhsa_exception_fp_ieee_inexact 0
		.amdhsa_exception_int_div_zero 0
	.end_amdhsa_kernel

.Lfunc_end0:
	.size	_Z6k_histPKfS0_S0_PfPiS1_, .Lfunc_end0-_Z6k_histPKfS0_S0_PfPiS1_
	.set _Z6k_histPKfS0_S0_PfPiS1_.num_vgpr, 66
	.set _Z6k_histPKfS0_S0_PfPiS1_.num_agpr, 0
	.set _Z6k_histPKfS0_S0_PfPiS1_.numbered_sgpr, 64
	.set _Z6k_histPKfS0_S0_PfPiS1_.num_named_barrier, 0
	.set _Z6k_histPKfS0_S0_PfPiS1_.private_seg_size, 0
	.set _Z6k_histPKfS0_S0_PfPiS1_.uses_vcc, 1
	.set _Z6k_histPKfS0_S0_PfPiS1_.uses_flat_scratch, 0
	.set _Z6k_histPKfS0_S0_PfPiS1_.has_dyn_sized_stack, 0
	.set _Z6k_histPKfS0_S0_PfPiS1_.has_recursion, 0
	.set _Z6k_histPKfS0_S0_PfPiS1_.has_indirect_call, 0

amdhsa.kernels:
  - .agpr_count:     0
    .args:
      - .actual_access:  read_only
        .address_space:  global
        .offset:         0
        .size:           8
        .value_kind:     global_buffer
      - .actual_access:  read_only
        .address_space:  global
        .offset:         8
        .size:           8
        .value_kind:     global_buffer
      - .actual_access:  read_only
        .address_space:  global
        .offset:         16
        .size:           8
        .value_kind:     global_buffer
      - .actual_access:  write_only
        .address_space:  global
        .offset:         24
        .size:           8
        .value_kind:     global_buffer
      - .actual_access:  write_only
        .address_space:  global
        .offset:         32
        .size:           8
        .value_kind:     global_buffer
      - .actual_access:  write_only
        .address_space:  global
        .offset:         40
        .size:           8
        .value_kind:     global_buffer
    .group_segment_fixed_size: 32
    .kernarg_segment_align: 8
    .kernarg_segment_size: 48
    .language:       OpenCL C
    .language_version:
      - 2
      - 0
    .max_flat_workgroup_size: 1024
    .name:           _Z6k_histPKfS0_S0_PfPiS1_
    .private_segment_fixed_size: 0
    .sgpr_count:     70
    .sgpr_spill_count: 0
    .symbol:         _Z6k_histPKfS0_S0_PfPiS1_.kd
    .uniform_work_group_size: 1
    .uses_dynamic_stack: false
    .vgpr_count:     66
    .vgpr_spill_count: 0
    .wavefront_size: 64
  - .agpr_count:     0
    .args:
      - .actual_access:  read_only
        .address_space:  global
        .offset:         0
        .size:           8
        .value_kind:     global_buffer
      - .actual_access:  read_only
        .address_space:  global
        .offset:         8
        .size:           8
        .value_kind:     global_buffer
      - .address_space:  global
        .offset:         16
        .size:           8
        .value_kind:     global_buffer
    .group_segment_fixed_size: 2080
    .kernarg_segment_align: 8
    .kernarg_segment_size: 24
    .language:       OpenCL C
    .language_version:
      - 2
      - 0
    .max_flat_workgroup_size: 256
    .name:           _Z7k_finalPKfPKiPf
    .private_segment_fixed_size: 0
    .sgpr_count:     34
    .sgpr_spill_count: 0
    .symbol:         _Z7k_finalPKfPKiPf.kd
    .uniform_work_group_size: 1
    .uses_dynamic_stack: false
    .vgpr_count:     36
    .vgpr_spill_count: 0
    .wavefront_size: 64
